# P0 rms-row loop: hoisted 8 row-invariant gain loads out of loop (removes load-wait-store chains)
# speedup vs baseline: 1.0001x; 1.0001x over previous
.LBB0_33:
	s_or_b64 exec, exec, s[12:13]
	s_cmpk_gt_i32 s52, 0x3fff
	s_cbranch_scc1 .LBB0_36
	v_mbcnt_lo_u32_b32 v1, -1, 0
	v_mbcnt_hi_u32_b32 v2, -1, v1
	v_and_b32_e32 v1, 64, v2
	v_add_u32_e32 v3, 64, v1
	v_xor_b32_e32 v1, 1, v2
	v_cmp_lt_i32_e32 vcc, v1, v3
	v_xor_b32_e32 v4, 2, v2
	s_ashr_i32 s53, s52, 31
	v_cndmask_b32_e32 v1, v2, v1, vcc
	v_cmp_lt_i32_e32 vcc, v4, v3
	s_mov_b64 s[0:1], 0x1000
	v_lshlrev_b32_e32 v1, 2, v1
	v_cndmask_b32_e32 v4, v2, v4, vcc
	v_lshlrev_b32_e32 v44, 2, v4
	v_xor_b32_e32 v4, 4, v2
	v_cmp_lt_i32_e32 vcc, v4, v3
	v_mov_b32_e32 v49, 0x3727c5ac
	v_mov_b32_e32 v50, 0x260
	v_cndmask_b32_e32 v4, v2, v4, vcc
	v_lshlrev_b32_e32 v45, 2, v4
	v_xor_b32_e32 v4, 8, v2
	v_cmp_lt_i32_e32 vcc, v4, v3
	s_nop 1
	v_cndmask_b32_e32 v4, v2, v4, vcc
	v_lshlrev_b32_e32 v46, 2, v4
	v_xor_b32_e32 v4, 16, v2
	v_cmp_lt_i32_e32 vcc, v4, v3
	s_nop 1
	v_cndmask_b32_e32 v4, v2, v4, vcc
	v_lshlrev_b32_e32 v47, 2, v4
	v_xor_b32_e32 v4, 32, v2
	v_cmp_lt_i32_e32 vcc, v4, v3
	v_mov_b32_e32 v3, 0
	v_mov_b32_e32 v5, v3
	v_cndmask_b32_e32 v2, v2, v4, vcc
	v_lshlrev_b32_e32 v48, 2, v2
	v_lshlrev_b32_e32 v2, 4, v162
	s_waitcnt vmcnt(4)
	v_lshl_add_u64 v[30:31], s[6:7], 0, v[2:3]
	s_mov_b64 s[6:7], 0x1400
	v_lshl_add_u64 v[34:35], v[30:31], 0, s[6:7]
	s_mov_b64 s[6:7], 0x1800
	v_lshl_add_u64 v[36:37], v[30:31], 0, s[6:7]
	s_mov_b64 s[6:7], 0x1c00
	v_lshl_add_u64 v[38:39], v[30:31], 0, s[6:7]
	s_lshl_b64 s[6:7], s[52:53], 12
	s_add_u32 s2, s2, s6
	v_lshlrev_b32_e32 v4, 3, v162
	s_addc_u32 s3, s3, s7
	v_lshl_add_u64 v[4:5], s[2:3], 0, v[4:5]
	s_mov_b64 s[2:3], 0x2600000
	s_ashr_i32 s55, s54, 31
	v_lshl_add_u64 v[40:41], v[4:5], 0, s[2:3]
	s_lshl_b64 s[6:7], s[54:55], 12
	s_lshl_b64 s[2:3], s[52:53], 13
	s_add_u32 s2, s4, s2
	s_addc_u32 s3, s5, s3
	v_lshl_add_u64 v[2:3], s[2:3], 0, v[2:3]
	v_lshl_add_u64 v[32:33], v[30:31], 0, s[0:1]
	v_lshl_add_u64 v[42:43], v[2:3], 0, s[0:1]
	s_lshl_b64 s[4:5], s[54:55], 13
	s_mov_b32 s0, 0xf800000
	s_mov_b32 s1, s52
	global_load_dwordx4 v[100:103], v[30:31], off
	global_load_dwordx4 v[104:107], v[30:31], off offset:1024
	global_load_dwordx4 v[108:111], v[30:31], off offset:2048
	global_load_dwordx4 v[112:115], v[30:31], off offset:3072
	global_load_dwordx4 v[116:119], v[32:33], off
	global_load_dwordx4 v[120:123], v[34:35], off
	global_load_dwordx4 v[124:127], v[36:37], off
	global_load_dwordx4 v[128:131], v[38:39], off
.LBB0_35:
	global_load_dwordx4 v[22:25], v[42:43], off offset:-4096
	global_load_dwordx4 v[6:9], v[42:43], off offset:-3072
	global_load_dwordx4 v[18:21], v[42:43], off offset:-2048
	global_load_dwordx4 v[10:13], v[42:43], off offset:1024
	global_load_dwordx4 v[26:29], v[42:43], off
	global_load_dwordx4 v[52:55], v[42:43], off offset:-1024
	global_load_dwordx4 v[2:5], v[42:43], off offset:3072
	global_load_dwordx4 v[14:17], v[42:43], off offset:2048
	s_add_i32 s1, s1, s54
	v_lshl_add_u64 v[42:43], v[42:43], 0, s[4:5]
	s_cmpk_lt_i32 s1, 0x4000
	s_waitcnt vmcnt(7)
	v_mov_b32_e32 v62, v23
	s_waitcnt vmcnt(6)
	v_mov_b32_e32 v63, v7
	v_mov_b32_e32 v66, v25
	v_mov_b32_e32 v67, v9
	v_mov_b32_e32 v60, v22
	v_mov_b32_e32 v61, v6
	v_mov_b32_e32 v64, v24
	v_mov_b32_e32 v65, v8
	s_waitcnt vmcnt(5)
	v_pk_mul_f32 v[68:69], v[20:21], v[20:21]
	v_pk_mul_f32 v[70:71], v[18:19], v[18:19]
	v_pk_mul_f32 v[62:63], v[62:63], v[62:63]
	v_pk_mul_f32 v[66:67], v[66:67], v[66:67]
	v_pk_mov_b32 v[84:85], v[70:71], v[68:69] op_sel:[1,0]
	v_mov_b32_e32 v71, v69
	v_pk_fma_f32 v[60:61], v[60:61], v[60:61], v[62:63]
	v_pk_fma_f32 v[62:63], v[64:65], v[64:65], v[66:67]
	s_waitcnt vmcnt(4)
	v_pk_mul_f32 v[72:73], v[12:13], v[12:13]
	v_pk_mul_f32 v[74:75], v[10:11], v[10:11]
	s_waitcnt vmcnt(2)
	v_mul_f32_e32 v76, v53, v53
	v_mul_f32_e32 v78, v55, v55
	v_pk_add_f32 v[64:65], v[84:85], v[70:71]
	v_pk_add_f32 v[60:61], v[60:61], v[62:63]
	v_mul_f32_e32 v51, v26, v26
	v_mul_f32_e32 v83, v27, v27
	v_mul_f32_e32 v86, v28, v28
	v_mul_f32_e32 v87, v29, v29
	v_pk_mov_b32 v[68:69], v[74:75], v[72:73] op_sel:[1,0]
	v_mov_b32_e32 v75, v73
	v_pk_fma_f32 v[72:73], v[52:53], v[52:53], v[76:77] op_sel_hi:[1,1,0]
	v_pk_fma_f32 v[76:77], v[54:55], v[54:55], v[78:79] op_sel_hi:[1,1,0]
	v_pk_add_f32 v[62:63], v[64:65], v[64:65] op_sel:[0,1] op_sel_hi:[1,0]
	v_pk_add_f32 v[60:61], v[60:61], v[60:61] op_sel:[0,1] op_sel_hi:[1,0]
	v_mov_b32_e32 v73, v86
	v_mov_b32_e32 v77, v87
	v_mov_b32_e32 v63, v83
	v_mov_b32_e32 v61, v51
	v_pk_add_f32 v[64:65], v[72:73], v[76:77]
	v_pk_add_f32 v[60:61], v[60:61], v[62:63]
	s_waitcnt vmcnt(0)
	v_mul_f32_e32 v80, v15, v15
	v_mul_f32_e32 v82, v17, v17
	v_pk_add_f32 v[66:67], v[68:69], v[74:75]
	v_pk_add_f32 v[60:61], v[60:61], v[64:65]
	v_mul_f32_e32 v88, v2, v2
	v_mul_f32_e32 v89, v4, v4
	v_mul_f32_e32 v90, v5, v5
	v_mul_f32_e32 v91, v3, v3
	v_pk_fma_f32 v[78:79], v[14:15], v[14:15], v[80:81] op_sel_hi:[1,1,0]
	v_pk_fma_f32 v[80:81], v[16:17], v[16:17], v[82:83] op_sel_hi:[1,1,0]
	v_pk_add_f32 v[66:67], v[66:67], v[66:67] op_sel:[0,1] op_sel_hi:[1,0]
	v_pk_add_f32 v[60:61], v[60:61], v[60:61] op_sel:[0,1] op_sel_hi:[1,0]
	v_mov_b32_e32 v79, v89
	v_mov_b32_e32 v81, v90
	v_mov_b32_e32 v67, v91
	v_mov_b32_e32 v61, v88
	v_pk_add_f32 v[68:69], v[78:79], v[80:81]
	v_pk_add_f32 v[60:61], v[60:61], v[66:67]
	s_nop 0
	v_pk_add_f32 v[60:61], v[60:61], v[68:69]
	s_nop 0
	v_add_f32_e32 v51, v60, v61
	ds_bpermute_b32 v60, v1, v51
	s_waitcnt lgkmcnt(0)
	v_add_f32_e32 v51, v51, v60
	ds_bpermute_b32 v60, v44, v51
	s_waitcnt lgkmcnt(0)
	v_add_f32_e32 v51, v51, v60
	ds_bpermute_b32 v60, v45, v51
	s_waitcnt lgkmcnt(0)
	v_add_f32_e32 v51, v51, v60
	ds_bpermute_b32 v60, v46, v51
	s_waitcnt lgkmcnt(0)
	v_add_f32_e32 v51, v51, v60
	ds_bpermute_b32 v60, v47, v51
	s_waitcnt lgkmcnt(0)
	v_add_f32_e32 v51, v51, v60
	ds_bpermute_b32 v60, v48, v51
	s_waitcnt lgkmcnt(0)
	v_add_f32_e32 v51, v51, v60
	v_fmamk_f32 v51, v51, 0x3a000000, v49
	v_mul_f32_e32 v60, 0x4f800000, v51
	v_cmp_gt_f32_e32 vcc, s0, v51
	s_nop 1
	v_cndmask_b32_e32 v51, v51, v60, vcc
	v_sqrt_f32_e32 v60, v51
	s_nop 0
	v_add_u32_e32 v61, -1, v60
	v_add_u32_e32 v62, 1, v60
	v_fma_f32 v63, -v61, v60, v51
	v_fma_f32 v64, -v62, v60, v51
	v_cmp_ge_f32_e64 s[2:3], 0, v63
	s_nop 1
	v_cndmask_b32_e64 v60, v60, v61, s[2:3]
	v_cmp_lt_f32_e64 s[2:3], 0, v64
	s_nop 1
	v_cndmask_b32_e64 v60, v60, v62, s[2:3]
	v_mul_f32_e32 v61, 0x37800000, v60
	v_cndmask_b32_e32 v60, v60, v61, vcc
	v_cmp_class_f32_e32 vcc, v51, v50
	s_nop 1
	v_cndmask_b32_e32 v51, v60, v51, vcc
	v_div_scale_f32 v60, s[2:3], v51, v51, 1.0
	v_rcp_f32_e32 v62, v60
	v_div_scale_f32 v61, vcc, 1.0, v51, 1.0
	v_fma_f32 v63, -v60, v62, 1.0
	v_fmac_f32_e32 v62, v63, v62
	v_mul_f32_e32 v63, v61, v62
	v_fma_f32 v64, -v60, v63, v61
	v_fmac_f32_e32 v63, v64, v62
	v_fma_f32 v60, -v60, v63, v61
	v_div_fmas_f32 v60, v60, v62, v63
	v_div_fixup_f32 v60, v60, v51, 1.0
	v_pk_mul_f32 v[22:23], v[22:23], v[60:61] op_sel_hi:[1,0]
	v_pk_mul_f32 v[24:25], v[24:25], v[60:61] op_sel_hi:[1,0]
	v_pk_mul_f32 v[22:23], v[100:101], v[22:23]
	v_pk_mul_f32 v[24:25], v[102:103], v[24:25]
	v_cvt_pk_bf16_f32 v22, v22, v23
	v_cvt_pk_bf16_f32 v23, v24, v25
	global_store_dwordx2 v[40:41], v[22:23], off
	s_nop 0
	v_pk_mul_f32 v[6:7], v[6:7], v[60:61] op_sel_hi:[1,0]
	v_pk_mul_f32 v[8:9], v[8:9], v[60:61] op_sel_hi:[1,0]
	v_pk_mul_f32 v[18:19], v[18:19], v[60:61] op_sel_hi:[1,0]
	v_pk_mul_f32 v[20:21], v[20:21], v[60:61] op_sel_hi:[1,0]
	v_pk_mul_f32 v[10:11], v[10:11], v[60:61] op_sel_hi:[1,0]
	v_pk_mul_f32 v[12:13], v[12:13], v[60:61] op_sel_hi:[1,0]
	v_pk_mul_f32 v[2:3], v[2:3], v[60:61] op_sel_hi:[1,0]
	v_pk_mul_f32 v[4:5], v[4:5], v[60:61] op_sel_hi:[1,0]
	v_pk_mul_f32 v[6:7], v[104:105], v[6:7]
	v_pk_mul_f32 v[8:9], v[106:107], v[8:9]
	v_cvt_pk_bf16_f32 v6, v6, v7
	v_cvt_pk_bf16_f32 v7, v8, v9
	global_store_dwordx2 v[40:41], v[6:7], off offset:512
	s_nop 0
	v_pk_mul_f32 v[6:7], v[108:109], v[18:19]
	v_pk_mul_f32 v[8:9], v[110:111], v[20:21]
	v_cvt_pk_bf16_f32 v6, v6, v7
	v_cvt_pk_bf16_f32 v7, v8, v9
	global_store_dwordx2 v[40:41], v[6:7], off offset:1024
	s_nop 0
	v_pk_mul_f32 v[18:19], v[52:53], v[60:61] op_sel_hi:[1,0]
	v_pk_mul_f32 v[20:21], v[54:55], v[60:61] op_sel_hi:[1,0]
	v_pk_mul_f32 v[6:7], v[112:113], v[18:19]
	v_pk_mul_f32 v[8:9], v[114:115], v[20:21]
	v_cvt_pk_bf16_f32 v6, v6, v7
	v_cvt_pk_bf16_f32 v7, v8, v9
	global_store_dwordx2 v[40:41], v[6:7], off offset:1536
	s_nop 0
	v_pk_mul_f32 v[18:19], v[26:27], v[60:61] op_sel_hi:[1,0]
	v_pk_mul_f32 v[20:21], v[28:29], v[60:61] op_sel_hi:[1,0]
	v_pk_mul_f32 v[6:7], v[18:19], v[116:117]
	v_pk_mul_f32 v[8:9], v[20:21], v[118:119]
	v_cvt_pk_bf16_f32 v6, v6, v7
	v_cvt_pk_bf16_f32 v7, v8, v9
	global_store_dwordx2 v[40:41], v[6:7], off offset:2048
	s_nop 0
	v_pk_mul_f32 v[6:7], v[10:11], v[120:121]
	v_pk_mul_f32 v[8:9], v[12:13], v[122:123]
	v_cvt_pk_bf16_f32 v6, v6, v7
	v_cvt_pk_bf16_f32 v7, v8, v9
	global_store_dwordx2 v[40:41], v[6:7], off offset:2560
	s_nop 0
	v_pk_mul_f32 v[10:11], v[14:15], v[60:61] op_sel_hi:[1,0]
	v_pk_mul_f32 v[12:13], v[16:17], v[60:61] op_sel_hi:[1,0]
	v_pk_mul_f32 v[6:7], v[10:11], v[124:125]
	v_pk_mul_f32 v[8:9], v[12:13], v[126:127]
	v_cvt_pk_bf16_f32 v6, v6, v7
	v_cvt_pk_bf16_f32 v7, v8, v9
	global_store_dwordx2 v[40:41], v[6:7], off offset:3072
	s_nop 0
	v_pk_mul_f32 v[2:3], v[2:3], v[128:129]
	v_pk_mul_f32 v[4:5], v[4:5], v[130:131]
	v_cvt_pk_bf16_f32 v2, v2, v3
	v_cvt_pk_bf16_f32 v3, v4, v5
	global_store_dwordx2 v[40:41], v[2:3], off offset:3584
	v_lshl_add_u64 v[40:41], v[40:41], 0, s[6:7]
	s_cbranch_scc1 .LBB0_35
